# speedup vs baseline: 1.0105x; 1.0033x over previous
.LBB3_6:
	ds_read_b128 v[2:5], v89 offset:32768
	ds_read_b128 v[22:25], v89 offset:33792
	s_xor_b64 s[8:9], s[4:5], -1
	s_mov_b64 s[6:7], -1
	s_mov_b64 s[4:5], 0
	s_waitcnt lgkmcnt(1)
	v_mfma_f32_32x32x16_f16 v[2:17], v[2:5], v[72:75], 0
	s_and_b64 vcc, exec, s[8:9]
	s_waitcnt lgkmcnt(0)
	v_mfma_f32_32x32x16_f16 v[2:17], v[22:25], v[76:79], v[2:17]
	ds_read_b128 v[22:25], v89 offset:36864
	ds_read_b128 v[106:109], v89 offset:37888
	ds_read_b128 v[110:113], v89 offset:34816
	ds_read_b128 v[114:117], v89 offset:38912
	ds_read_b128 v[118:121], v89 offset:35840
	s_waitcnt lgkmcnt(4)
	v_mfma_f32_32x32x16_f16 v[24:39], v[22:25], v[72:75], 0
	s_waitcnt lgkmcnt(3)
	v_mfma_f32_32x32x16_f16 v[24:39], v[106:109], v[76:79], v[24:39]
	s_waitcnt lgkmcnt(2)
	v_mfma_f32_32x32x16_f16 v[2:17], v[110:113], v[80:83], v[2:17]
	s_waitcnt lgkmcnt(1)
	v_mfma_f32_32x32x16_f16 v[24:39], v[114:117], v[80:83], v[24:39]
	s_cmp_eq_u64 s[8:9], 0
	s_cbranch_scc0 .Lmy_attn_nodma
	s_mov_b32 m0, s48
	s_nop 0
	global_load_lds_dwordx4 v88, s[52:53]
	s_add_u32 s54, s52, 0x2000
	s_addc_u32 s55, s53, 0
	s_add_u32 m0, s48, 0x2000
	s_nop 0
	global_load_lds_dwordx4 v88, s[54:55]
	s_add_u32 s54, s52, 0x4000
	s_addc_u32 s55, s53, 0
	s_add_u32 m0, s48, 0x4000
	s_nop 0
	global_load_lds_dwordx4 v88, s[54:55]
	s_add_u32 s54, s52, 0x6000
	s_addc_u32 s55, s53, 0
	s_add_u32 m0, s48, 0x6000
	s_nop 0
	global_load_lds_dwordx4 v88, s[54:55]
	s_branch .Lmy_attn_dmadone
.Lmy_attn_nodma:
	s_nop 9
.Lmy_attn_dmadone:
	v_exp_f32_e32 v2, v2
	v_exp_f32_e32 v22, v3
	v_exp_f32_e32 v3, v4
	v_exp_f32_e32 v23, v5
	v_exp_f32_e32 v4, v6
	v_exp_f32_e32 v6, v7
	v_exp_f32_e32 v5, v8
	v_exp_f32_e32 v7, v9
	v_exp_f32_e32 v10, v10
	v_exp_f32_e32 v11, v11
	v_exp_f32_e32 v12, v12
	v_exp_f32_e32 v13, v13
	v_exp_f32_e32 v8, v14
	v_exp_f32_e32 v14, v15
	v_exp_f32_e32 v9, v16
	v_exp_f32_e32 v15, v17
	v_cvt_pk_bf16_f32 v5, v5, v7
	v_cvt_pk_bf16_f32 v4, v4, v6
	v_cvt_pk_bf16_f32 v3, v3, v23
	v_cvt_pk_bf16_f32 v2, v2, v22
	v_cvt_pk_bf16_f32 v9, v9, v15
	v_cvt_pk_bf16_f32 v8, v8, v14
	v_cvt_pk_bf16_f32 v7, v12, v13
	v_cvt_pk_bf16_f32 v6, v10, v11
	s_nop 1
	v_permlane16_swap_b32_e32 v2, v6
	v_permlane16_swap_b32_e32 v3, v7
	v_permlane16_swap_b32_e32 v4, v8
	v_permlane16_swap_b32_e32 v5, v9
	v_exp_f32_e32 v114, v24
	v_exp_f32_e32 v22, v26
	v_exp_f32_e32 v23, v28
	v_exp_f32_e32 v24, v30
	s_waitcnt lgkmcnt(0)
	v_mfma_f32_16x16x32_bf16 v[6:9], v[118:121], v[6:9], v[18:21]
	ds_read_b128 v[10:13], v89 offset:39936
	ds_read_b128 v[14:17], v89 offset:40960
	ds_read_b128 v[106:109], v89 offset:41984
	ds_read_b128 v[110:113], v89 offset:43008
	v_exp_f32_e32 v18, v31
	v_exp_f32_e32 v19, v29
	v_exp_f32_e32 v20, v27
	v_mfma_f32_16x16x32_bf16 v[2:5], v[118:121], v[2:5], v[84:87]
	s_nop 2
	v_exp_f32_e32 v84, v25
	v_cvt_pk_bf16_f32 v87, v24, v18
	v_cvt_pk_bf16_f32 v86, v23, v19
	v_cvt_pk_bf16_f32 v85, v22, v20
	s_waitcnt lgkmcnt(2)
	v_mfma_f32_32x32x16_f16 v[16:31], v[14:17], v[72:75], 0
	v_exp_f32_e32 v14, v32
	v_exp_f32_e32 v15, v34
	v_exp_f32_e32 v32, v36
	v_exp_f32_e32 v34, v37
	v_exp_f32_e32 v36, v38
	v_exp_f32_e32 v37, v39
	v_exp_f32_e32 v38, v35
	s_waitcnt lgkmcnt(1)
	v_mfma_f32_32x32x16_f16 v[16:31], v[106:109], v[76:79], v[16:31]
	v_exp_f32_e32 v39, v33
	v_cvt_pk_bf16_f32 v84, v114, v84
	v_cvt_pk_bf16_f32 v35, v36, v37
	v_cvt_pk_bf16_f32 v34, v32, v34
	v_cvt_pk_bf16_f32 v33, v15, v38
	v_cvt_pk_bf16_f32 v32, v14, v39
	s_nop 1
	v_permlane16_swap_b32_e32 v84, v32
	v_permlane16_swap_b32_e32 v85, v33
	v_permlane16_swap_b32_e32 v86, v34
	v_permlane16_swap_b32_e32 v87, v35
	ds_read_b128 v[36:39], v89 offset:44032
	s_nop 0
	v_mfma_f32_16x16x32_bf16 v[84:87], v[10:13], v[84:87], v[2:5]
	s_nop 2
	ds_read_b128 v[2:5], v89 offset:45056
	s_waitcnt lgkmcnt(2)
	v_mfma_f32_32x32x16_f16 v[16:31], v[110:113], v[80:83], v[16:31]
	v_mfma_f32_16x16x32_bf16 v[106:109], v[10:13], v[32:35], v[6:9]
	s_nop 10
	v_exp_f32_e32 v114, v16
	v_exp_f32_e32 v118, v17
	v_exp_f32_e32 v18, v18
	s_waitcnt lgkmcnt(0)
	v_mfma_f32_32x32x16_f16 v[2:17], v[2:5], v[72:75], 0
	v_exp_f32_e32 v20, v20
	v_exp_f32_e32 v21, v21
	v_exp_f32_e32 v19, v19
	ds_read_b128 v[32:35], v89 offset:46080
	ds_read_b128 v[110:113], v89 offset:47104
	v_cvt_pk_bf16_f32 v114, v114, v118
	v_cvt_pk_bf16_f32 v116, v20, v21
	v_cvt_pk_bf16_f32 v115, v18, v19
	ds_read_b128 v[118:121], v89 offset:48128
	ds_read_b128 v[18:21], v89 offset:49152
	v_exp_f32_e32 v22, v22
	v_exp_f32_e32 v23, v23
	s_waitcnt lgkmcnt(3)
	v_mfma_f32_32x32x16_f16 v[2:17], v[32:35], v[76:79], v[2:17]
	v_exp_f32_e32 v29, v29
	v_exp_f32_e32 v27, v27
	v_cvt_pk_bf16_f32 v117, v22, v23
	v_exp_f32_e32 v22, v24
	v_exp_f32_e32 v23, v26
	v_exp_f32_e32 v24, v28
	v_exp_f32_e32 v26, v30
	v_exp_f32_e32 v28, v31
	v_exp_f32_e32 v25, v25
	ds_read_b128 v[122:125], v89 offset:50176
	s_waitcnt lgkmcnt(3)
	v_mfma_f32_32x32x16_f16 v[2:17], v[110:113], v[80:83], v[2:17]
	v_cvt_pk_bf16_f32 v113, v26, v28
	v_cvt_pk_bf16_f32 v112, v24, v29
	v_cvt_pk_bf16_f32 v111, v23, v27
	v_cvt_pk_bf16_f32 v110, v22, v25
	s_nop 1
	v_permlane16_swap_b32_e32 v114, v110
	v_permlane16_swap_b32_e32 v115, v111
	s_waitcnt lgkmcnt(1)
	v_mfma_f32_32x32x16_f16 v[18:33], v[18:21], v[72:75], 0
	v_permlane16_swap_b32_e32 v116, v112
	v_permlane16_swap_b32_e32 v117, v113
	v_exp_f32_e32 v2, v2
	v_exp_f32_e32 v4, v4
	v_exp_f32_e32 v5, v5
	v_mfma_f32_16x16x32_bf16 v[84:87], v[36:39], v[114:117], v[84:87]
	v_exp_f32_e32 v3, v3
	v_exp_f32_e32 v6, v6
	v_exp_f32_e32 v7, v7
	v_mfma_f32_16x16x32_bf16 v[34:37], v[36:39], v[110:113], v[106:109]
	ds_read_b128 v[110:113], v89 offset:52224
	v_exp_f32_e32 v8, v8
	v_exp_f32_e32 v9, v9
	ds_read_b128 v[106:109], v89 offset:51200
	s_waitcnt lgkmcnt(2)
	v_mfma_f32_32x32x16_f16 v[18:33], v[122:125], v[76:79], v[18:33]
	v_exp_f32_e32 v13, v13
	v_exp_f32_e32 v11, v11
	ds_read_b128 v[122:125], v89 offset:54272
	s_waitcnt lgkmcnt(1)
	v_mfma_f32_32x32x16_f16 v[18:33], v[106:109], v[80:83], v[18:33]
	v_cvt_pk_bf16_f32 v107, v4, v5
	v_cvt_pk_bf16_f32 v106, v2, v3
	ds_read_b128 v[2:5], v89 offset:53248
	v_cvt_pk_bf16_f32 v109, v8, v9
	v_cvt_pk_bf16_f32 v108, v6, v7
	v_exp_f32_e32 v6, v10
	v_exp_f32_e32 v7, v12
	v_exp_f32_e32 v8, v14
	v_exp_f32_e32 v9, v16
	v_exp_f32_e32 v10, v17
	v_exp_f32_e32 v12, v15
	v_cvt_pk_bf16_f32 v115, v7, v13
	v_cvt_pk_bf16_f32 v114, v6, v11
	v_cvt_pk_bf16_f32 v117, v9, v10
	v_cvt_pk_bf16_f32 v116, v8, v12
	s_waitcnt lgkmcnt(0)
	v_mfma_f32_32x32x16_f16 v[2:17], v[2:5], v[72:75], 0
	v_permlane16_swap_b32_e32 v106, v114
	v_permlane16_swap_b32_e32 v107, v115
	v_permlane16_swap_b32_e32 v108, v116
	v_permlane16_swap_b32_e32 v109, v117
	v_mfma_f32_32x32x16_f16 v[2:17], v[122:125], v[76:79], v[2:17]
	v_exp_f32_e32 v18, v18
	v_exp_f32_e32 v20, v20
	v_exp_f32_e32 v21, v21
	v_exp_f32_e32 v19, v19
	v_exp_f32_e32 v22, v22
	v_exp_f32_e32 v24, v24
	v_exp_f32_e32 v25, v25
	v_mfma_f32_16x16x32_bf16 v[84:87], v[118:121], v[106:109], v[84:87]
	v_exp_f32_e32 v23, v23
	v_exp_f32_e32 v29, v29
	v_exp_f32_e32 v27, v27
	v_mfma_f32_16x16x32_bf16 v[34:37], v[118:121], v[114:117], v[34:37]
	ds_read_b128 v[106:109], v89 offset:55296
	ds_read_b128 v[114:117], v89 offset:56320
	ds_read_b128 v[122:125], v89 offset:58368
	s_waitcnt lgkmcnt(2)
	v_mfma_f32_32x32x16_f16 v[2:17], v[106:109], v[80:83], v[2:17]
	v_cvt_pk_bf16_f32 v107, v20, v21
	v_cvt_pk_bf16_f32 v106, v18, v19
	ds_read_b128 v[18:21], v89 offset:57344
	v_cvt_pk_bf16_f32 v109, v24, v25
	v_cvt_pk_bf16_f32 v108, v22, v23
	v_exp_f32_e32 v22, v26
	v_exp_f32_e32 v23, v28
	v_exp_f32_e32 v24, v30
	v_exp_f32_e32 v25, v32
	v_exp_f32_e32 v26, v33
	v_exp_f32_e32 v28, v31
	v_cvt_pk_bf16_f32 v119, v23, v29
	v_cvt_pk_bf16_f32 v118, v22, v27
	v_cvt_pk_bf16_f32 v121, v25, v26
	v_cvt_pk_bf16_f32 v120, v24, v28
	s_waitcnt lgkmcnt(0)
	v_mfma_f32_32x32x16_f16 v[18:33], v[18:21], v[72:75], 0
	v_permlane16_swap_b32_e32 v106, v118
	v_permlane16_swap_b32_e32 v107, v119
	v_permlane16_swap_b32_e32 v108, v120
	v_permlane16_swap_b32_e32 v109, v121
	v_mfma_f32_32x32x16_f16 v[18:33], v[122:125], v[76:79], v[18:33]
	v_exp_f32_e32 v2, v2
	v_exp_f32_e32 v4, v4
	v_exp_f32_e32 v5, v5
	v_exp_f32_e32 v3, v3
	v_exp_f32_e32 v6, v6
	v_exp_f32_e32 v8, v8
	v_exp_f32_e32 v9, v9
	v_mfma_f32_16x16x32_bf16 v[84:87], v[110:113], v[106:109], v[84:87]
	v_exp_f32_e32 v7, v7
	v_exp_f32_e32 v13, v13
	v_exp_f32_e32 v11, v11
	v_mfma_f32_16x16x32_bf16 v[34:37], v[110:113], v[118:121], v[34:37]
	ds_read_b128 v[106:109], v89 offset:59392
	ds_read_b128 v[110:113], v89 offset:60416
	ds_read_b128 v[122:125], v89 offset:62464
	s_waitcnt lgkmcnt(2)
	v_mfma_f32_32x32x16_f16 v[18:33], v[106:109], v[80:83], v[18:33]
	v_cvt_pk_bf16_f32 v107, v4, v5
	v_cvt_pk_bf16_f32 v106, v2, v3
	ds_read_b128 v[2:5], v89 offset:61440
	v_cvt_pk_bf16_f32 v109, v8, v9
	v_cvt_pk_bf16_f32 v108, v6, v7
	v_exp_f32_e32 v6, v10
	v_exp_f32_e32 v7, v12
	v_exp_f32_e32 v8, v14
	v_exp_f32_e32 v9, v16
	v_exp_f32_e32 v10, v17
	v_exp_f32_e32 v12, v15
	v_cvt_pk_bf16_f32 v119, v7, v13
	v_cvt_pk_bf16_f32 v118, v6, v11
	v_cvt_pk_bf16_f32 v121, v9, v10
	v_cvt_pk_bf16_f32 v120, v8, v12
	s_waitcnt lgkmcnt(0)
	v_mfma_f32_32x32x16_f16 v[2:17], v[2:5], v[72:75], 0
	v_permlane16_swap_b32_e32 v106, v118
	v_permlane16_swap_b32_e32 v107, v119
	v_permlane16_swap_b32_e32 v108, v120
	v_permlane16_swap_b32_e32 v109, v121
	v_mfma_f32_32x32x16_f16 v[2:17], v[122:125], v[76:79], v[2:17]
	v_exp_f32_e32 v38, v20
	v_exp_f32_e32 v20, v22
	v_exp_f32_e32 v22, v24
	v_exp_f32_e32 v24, v25
	v_exp_f32_e32 v25, v21
	v_exp_f32_e32 v23, v23
	v_exp_f32_e32 v39, v19
	v_mfma_f32_16x16x32_bf16 v[84:87], v[114:117], v[106:109], v[84:87]
	v_cvt_pk_bf16_f32 v21, v22, v24
	v_cvt_pk_bf16_f32 v19, v38, v25
	v_exp_f32_e32 v22, v26
	v_mfma_f32_16x16x32_bf16 v[34:37], v[114:117], v[118:121], v[34:37]
	ds_read_b128 v[106:109], v89 offset:63488
	ds_read_b128 v[114:117], v89 offset:64512
	v_exp_f32_e32 v25, v32
	v_exp_f32_e32 v26, v33
	s_waitcnt lgkmcnt(1)
	v_mfma_f32_32x32x16_f16 v[2:17], v[106:109], v[80:83], v[2:17]
	v_exp_f32_e32 v18, v18
	v_cvt_pk_bf16_f32 v20, v20, v23
	v_exp_f32_e32 v23, v28
	v_exp_f32_e32 v24, v30
	v_exp_f32_e32 v28, v31
	v_exp_f32_e32 v29, v29
	v_exp_f32_e32 v27, v27
	v_cvt_pk_bf16_f32 v25, v25, v26
	s_nop 3
	v_exp_f32_e32 v26, v4
	v_exp_f32_e32 v4, v6
	v_exp_f32_e32 v6, v8
	v_exp_f32_e32 v8, v9
	v_exp_f32_e32 v7, v7
	v_exp_f32_e32 v9, v5
	v_cvt_pk_bf16_f32 v18, v18, v39
	v_cvt_pk_bf16_f32 v24, v24, v28
	v_cvt_pk_bf16_f32 v23, v23, v29
	v_cvt_pk_bf16_f32 v22, v22, v27
	v_exp_f32_e32 v2, v2
	v_exp_f32_e32 v27, v3
	v_cvt_pk_bf16_f32 v5, v6, v8
	v_cvt_pk_bf16_f32 v4, v4, v7
	v_cvt_pk_bf16_f32 v3, v26, v9
	v_exp_f32_e32 v6, v10
	v_exp_f32_e32 v7, v12
	v_exp_f32_e32 v8, v14
	v_exp_f32_e32 v9, v16
	v_exp_f32_e32 v10, v17
	v_exp_f32_e32 v12, v15
	v_exp_f32_e32 v13, v13
	v_exp_f32_e32 v11, v11
	v_permlane16_swap_b32_e32 v18, v22
	v_permlane16_swap_b32_e32 v19, v23
	v_permlane16_swap_b32_e32 v20, v24
	v_permlane16_swap_b32_e32 v21, v25
	v_cvt_pk_bf16_f32 v2, v2, v27
	s_nop 0
	v_mfma_f32_16x16x32_bf16 v[18:21], v[110:113], v[18:21], v[84:87]
	v_cvt_pk_bf16_f32 v9, v9, v10
	v_cvt_pk_bf16_f32 v8, v8, v12
	v_cvt_pk_bf16_f32 v7, v7, v13
	v_mfma_f32_16x16x32_bf16 v[22:25], v[110:113], v[22:25], v[34:37]
	v_cvt_pk_bf16_f32 v6, v6, v11
	s_nop 1
	v_permlane16_swap_b32_e32 v2, v6
	v_permlane16_swap_b32_e32 v3, v7
	v_permlane16_swap_b32_e32 v4, v8
	v_permlane16_swap_b32_e32 v5, v9
	s_waitcnt lgkmcnt(0)
	s_nop 0
	v_mfma_f32_16x16x32_bf16 v[84:87], v[114:117], v[2:5], v[18:21]
	s_waitcnt vmcnt(0)
	s_barrier
	v_mfma_f32_16x16x32_bf16 v[18:21], v[114:117], v[6:9], v[22:25]
	s_cbranch_vccnz .LBB3_13

.LBB3_9:
	ds_read_b128 v[2:5], v89
	ds_read_b128 v[22:25], v89 offset:1024
	s_xor_b64 s[6:7], s[6:7], -1
	s_andn2_b64 vcc, exec, s[6:7]
	s_waitcnt lgkmcnt(1)
	v_mfma_f32_32x32x16_f16 v[2:17], v[2:5], v[72:75], 0
	s_waitcnt lgkmcnt(0)
	v_mfma_f32_32x32x16_f16 v[2:17], v[22:25], v[76:79], v[2:17]
	ds_read_b128 v[22:25], v89 offset:4096
	ds_read_b128 v[106:109], v89 offset:5120
	ds_read_b128 v[110:113], v89 offset:2048
	ds_read_b128 v[114:117], v89 offset:6144
	ds_read_b128 v[118:121], v89 offset:3072
	s_waitcnt lgkmcnt(4)
	v_mfma_f32_32x32x16_f16 v[24:39], v[22:25], v[72:75], 0
	s_waitcnt lgkmcnt(3)
	v_mfma_f32_32x32x16_f16 v[24:39], v[106:109], v[76:79], v[24:39]
	s_waitcnt lgkmcnt(2)
	v_mfma_f32_32x32x16_f16 v[2:17], v[110:113], v[80:83], v[2:17]
	s_waitcnt lgkmcnt(1)
	v_mfma_f32_32x32x16_f16 v[24:39], v[114:117], v[80:83], v[24:39]
	s_add_u32 m0, s48, 0x8000
	s_nop 0
	global_load_lds_dwordx4 v88, s[50:51]
	s_add_u32 s54, s50, 0x2000
	s_addc_u32 s55, s51, 0
	s_add_u32 m0, s48, 0xa000
	s_nop 0
	global_load_lds_dwordx4 v88, s[54:55]
	s_add_u32 s54, s50, 0x4000
	s_addc_u32 s55, s51, 0
	s_add_u32 m0, s48, 0xc000
	s_nop 0
	global_load_lds_dwordx4 v88, s[54:55]
	s_add_u32 s54, s50, 0x6000
	s_addc_u32 s55, s51, 0
	s_add_u32 m0, s48, 0xe000
	s_nop 0
	global_load_lds_dwordx4 v88, s[54:55]
	s_add_u32 s50, s50, 0x10000
	s_addc_u32 s51, s51, 0
	v_exp_f32_e32 v2, v2
	v_exp_f32_e32 v22, v3
	v_exp_f32_e32 v3, v4
	v_exp_f32_e32 v23, v5
	v_exp_f32_e32 v4, v6
	v_exp_f32_e32 v6, v7
	v_exp_f32_e32 v5, v8
	v_exp_f32_e32 v7, v9
	v_exp_f32_e32 v10, v10
	v_exp_f32_e32 v11, v11
	v_exp_f32_e32 v12, v12
	v_exp_f32_e32 v13, v13
	v_exp_f32_e32 v8, v14
	v_exp_f32_e32 v14, v15
	v_exp_f32_e32 v9, v16
	v_exp_f32_e32 v15, v17
	v_cvt_pk_bf16_f32 v5, v5, v7
	v_cvt_pk_bf16_f32 v4, v4, v6
	v_cvt_pk_bf16_f32 v3, v3, v23
	v_cvt_pk_bf16_f32 v2, v2, v22
	v_cvt_pk_bf16_f32 v9, v9, v15
	v_cvt_pk_bf16_f32 v8, v8, v14
	v_cvt_pk_bf16_f32 v7, v12, v13
	v_cvt_pk_bf16_f32 v6, v10, v11
	s_nop 1
	v_permlane16_swap_b32_e32 v2, v6
	v_permlane16_swap_b32_e32 v3, v7
	v_permlane16_swap_b32_e32 v4, v8
	v_permlane16_swap_b32_e32 v5, v9
	v_exp_f32_e32 v114, v24
	v_exp_f32_e32 v22, v26
	v_exp_f32_e32 v23, v28
	v_exp_f32_e32 v24, v30
	s_waitcnt lgkmcnt(0)
	v_mfma_f32_16x16x32_bf16 v[6:9], v[118:121], v[6:9], v[18:21]
	ds_read_b128 v[10:13], v89 offset:7168
	ds_read_b128 v[14:17], v89 offset:8192
	ds_read_b128 v[106:109], v89 offset:9216
	ds_read_b128 v[110:113], v89 offset:10240
	v_exp_f32_e32 v18, v31
	v_exp_f32_e32 v19, v29
	v_exp_f32_e32 v20, v27
	v_mfma_f32_16x16x32_bf16 v[2:5], v[118:121], v[2:5], v[84:87]
	s_nop 2
	v_exp_f32_e32 v84, v25
	v_cvt_pk_bf16_f32 v87, v24, v18
	v_cvt_pk_bf16_f32 v86, v23, v19
	v_cvt_pk_bf16_f32 v85, v22, v20
	s_waitcnt lgkmcnt(2)
	v_mfma_f32_32x32x16_f16 v[16:31], v[14:17], v[72:75], 0
	v_exp_f32_e32 v14, v32
	v_exp_f32_e32 v15, v34
	v_exp_f32_e32 v32, v36
	v_exp_f32_e32 v34, v37
	v_exp_f32_e32 v36, v38
	v_exp_f32_e32 v37, v39
	v_exp_f32_e32 v38, v35
	s_waitcnt lgkmcnt(1)
	v_mfma_f32_32x32x16_f16 v[16:31], v[106:109], v[76:79], v[16:31]
	v_exp_f32_e32 v39, v33
	v_cvt_pk_bf16_f32 v84, v114, v84
	v_cvt_pk_bf16_f32 v35, v36, v37
	v_cvt_pk_bf16_f32 v34, v32, v34
	v_cvt_pk_bf16_f32 v33, v15, v38
	v_cvt_pk_bf16_f32 v32, v14, v39
	s_nop 1
	v_permlane16_swap_b32_e32 v84, v32
	v_permlane16_swap_b32_e32 v85, v33
	v_permlane16_swap_b32_e32 v86, v34
	v_permlane16_swap_b32_e32 v87, v35
	ds_read_b128 v[36:39], v89 offset:11264
	s_nop 0
	v_mfma_f32_16x16x32_bf16 v[84:87], v[10:13], v[84:87], v[2:5]
	s_nop 2
	ds_read_b128 v[2:5], v89 offset:12288
	s_waitcnt lgkmcnt(2)
	v_mfma_f32_32x32x16_f16 v[16:31], v[110:113], v[80:83], v[16:31]
	v_mfma_f32_16x16x32_bf16 v[106:109], v[10:13], v[32:35], v[6:9]
	s_nop 10
	v_exp_f32_e32 v114, v16
	v_exp_f32_e32 v118, v17
	v_exp_f32_e32 v18, v18
	s_waitcnt lgkmcnt(0)
	v_mfma_f32_32x32x16_f16 v[2:17], v[2:5], v[72:75], 0
	v_exp_f32_e32 v20, v20
	v_exp_f32_e32 v21, v21
	v_exp_f32_e32 v19, v19
	ds_read_b128 v[32:35], v89 offset:13312
	ds_read_b128 v[110:113], v89 offset:14336
	v_cvt_pk_bf16_f32 v114, v114, v118
	v_cvt_pk_bf16_f32 v116, v20, v21
	v_cvt_pk_bf16_f32 v115, v18, v19
	ds_read_b128 v[118:121], v89 offset:15360
	ds_read_b128 v[18:21], v89 offset:16384
	v_exp_f32_e32 v22, v22
	v_exp_f32_e32 v23, v23
	s_waitcnt lgkmcnt(3)
	v_mfma_f32_32x32x16_f16 v[2:17], v[32:35], v[76:79], v[2:17]
	v_exp_f32_e32 v29, v29
	v_exp_f32_e32 v27, v27
	v_cvt_pk_bf16_f32 v117, v22, v23
	v_exp_f32_e32 v22, v24
	v_exp_f32_e32 v23, v26
	v_exp_f32_e32 v24, v28
	v_exp_f32_e32 v26, v30
	v_exp_f32_e32 v28, v31
	v_exp_f32_e32 v25, v25
	ds_read_b128 v[122:125], v89 offset:17408
	s_waitcnt lgkmcnt(3)
	v_mfma_f32_32x32x16_f16 v[2:17], v[110:113], v[80:83], v[2:17]
	v_cvt_pk_bf16_f32 v113, v26, v28
	v_cvt_pk_bf16_f32 v112, v24, v29
	v_cvt_pk_bf16_f32 v111, v23, v27
	v_cvt_pk_bf16_f32 v110, v22, v25
	s_nop 1
	v_permlane16_swap_b32_e32 v114, v110
	v_permlane16_swap_b32_e32 v115, v111
	s_waitcnt lgkmcnt(1)
	v_mfma_f32_32x32x16_f16 v[18:33], v[18:21], v[72:75], 0
	v_permlane16_swap_b32_e32 v116, v112
	v_permlane16_swap_b32_e32 v117, v113
	v_exp_f32_e32 v2, v2
	v_exp_f32_e32 v4, v4
	v_exp_f32_e32 v5, v5
	v_mfma_f32_16x16x32_bf16 v[84:87], v[36:39], v[114:117], v[84:87]
	v_exp_f32_e32 v3, v3
	v_exp_f32_e32 v6, v6
	v_exp_f32_e32 v7, v7
	v_mfma_f32_16x16x32_bf16 v[34:37], v[36:39], v[110:113], v[106:109]
	ds_read_b128 v[110:113], v89 offset:19456
	v_exp_f32_e32 v8, v8
	v_exp_f32_e32 v9, v9
	ds_read_b128 v[106:109], v89 offset:18432
	s_waitcnt lgkmcnt(2)
	v_mfma_f32_32x32x16_f16 v[18:33], v[122:125], v[76:79], v[18:33]
	v_exp_f32_e32 v13, v13
	v_exp_f32_e32 v11, v11
	ds_read_b128 v[122:125], v89 offset:21504
	s_waitcnt lgkmcnt(1)
	v_mfma_f32_32x32x16_f16 v[18:33], v[106:109], v[80:83], v[18:33]
	v_cvt_pk_bf16_f32 v107, v4, v5
	v_cvt_pk_bf16_f32 v106, v2, v3
	ds_read_b128 v[2:5], v89 offset:20480
	v_cvt_pk_bf16_f32 v109, v8, v9
	v_cvt_pk_bf16_f32 v108, v6, v7
	v_exp_f32_e32 v6, v10
	v_exp_f32_e32 v7, v12
	v_exp_f32_e32 v8, v14
	v_exp_f32_e32 v9, v16
	v_exp_f32_e32 v10, v17
	v_exp_f32_e32 v12, v15
	v_cvt_pk_bf16_f32 v115, v7, v13
	v_cvt_pk_bf16_f32 v114, v6, v11
	v_cvt_pk_bf16_f32 v117, v9, v10
	v_cvt_pk_bf16_f32 v116, v8, v12
	s_waitcnt lgkmcnt(0)
	v_mfma_f32_32x32x16_f16 v[2:17], v[2:5], v[72:75], 0
	v_permlane16_swap_b32_e32 v106, v114
	v_permlane16_swap_b32_e32 v107, v115
	v_permlane16_swap_b32_e32 v108, v116
	v_permlane16_swap_b32_e32 v109, v117
	v_mfma_f32_32x32x16_f16 v[2:17], v[122:125], v[76:79], v[2:17]
	v_exp_f32_e32 v18, v18
	v_exp_f32_e32 v20, v20
	v_exp_f32_e32 v21, v21
	v_exp_f32_e32 v19, v19
	v_exp_f32_e32 v22, v22
	v_exp_f32_e32 v24, v24
	v_exp_f32_e32 v25, v25
	v_mfma_f32_16x16x32_bf16 v[84:87], v[118:121], v[106:109], v[84:87]
	v_exp_f32_e32 v23, v23
	v_exp_f32_e32 v29, v29
	v_exp_f32_e32 v27, v27
	v_mfma_f32_16x16x32_bf16 v[34:37], v[118:121], v[114:117], v[34:37]
	ds_read_b128 v[106:109], v89 offset:22528
	ds_read_b128 v[114:117], v89 offset:23552
	ds_read_b128 v[122:125], v89 offset:25600
	s_waitcnt lgkmcnt(2)
	v_mfma_f32_32x32x16_f16 v[2:17], v[106:109], v[80:83], v[2:17]
	v_cvt_pk_bf16_f32 v107, v20, v21
	v_cvt_pk_bf16_f32 v106, v18, v19
	ds_read_b128 v[18:21], v89 offset:24576
	v_cvt_pk_bf16_f32 v109, v24, v25
	v_cvt_pk_bf16_f32 v108, v22, v23
	v_exp_f32_e32 v22, v26
	v_exp_f32_e32 v23, v28
	v_exp_f32_e32 v24, v30
	v_exp_f32_e32 v25, v32
	v_exp_f32_e32 v26, v33
	v_exp_f32_e32 v28, v31
	v_cvt_pk_bf16_f32 v119, v23, v29
	v_cvt_pk_bf16_f32 v118, v22, v27
	v_cvt_pk_bf16_f32 v121, v25, v26
	v_cvt_pk_bf16_f32 v120, v24, v28
	s_waitcnt lgkmcnt(0)
	v_mfma_f32_32x32x16_f16 v[18:33], v[18:21], v[72:75], 0
	v_permlane16_swap_b32_e32 v106, v118
	v_permlane16_swap_b32_e32 v107, v119
	v_permlane16_swap_b32_e32 v108, v120
	v_permlane16_swap_b32_e32 v109, v121
	v_mfma_f32_32x32x16_f16 v[18:33], v[122:125], v[76:79], v[18:33]
	v_exp_f32_e32 v2, v2
	v_exp_f32_e32 v4, v4
	v_exp_f32_e32 v5, v5
	v_exp_f32_e32 v3, v3
	v_exp_f32_e32 v6, v6
	v_exp_f32_e32 v8, v8
	v_exp_f32_e32 v9, v9
	v_mfma_f32_16x16x32_bf16 v[84:87], v[110:113], v[106:109], v[84:87]
	v_exp_f32_e32 v7, v7
	v_exp_f32_e32 v13, v13
	v_exp_f32_e32 v11, v11
	v_mfma_f32_16x16x32_bf16 v[34:37], v[110:113], v[118:121], v[34:37]
	ds_read_b128 v[106:109], v89 offset:26624
	ds_read_b128 v[110:113], v89 offset:27648
	ds_read_b128 v[122:125], v89 offset:29696
	s_waitcnt lgkmcnt(2)
	v_mfma_f32_32x32x16_f16 v[18:33], v[106:109], v[80:83], v[18:33]
	v_cvt_pk_bf16_f32 v107, v4, v5
	v_cvt_pk_bf16_f32 v106, v2, v3
	ds_read_b128 v[2:5], v89 offset:28672
	v_cvt_pk_bf16_f32 v109, v8, v9
	v_cvt_pk_bf16_f32 v108, v6, v7
	v_exp_f32_e32 v6, v10
	v_exp_f32_e32 v7, v12
	v_exp_f32_e32 v8, v14
	v_exp_f32_e32 v9, v16
	v_exp_f32_e32 v10, v17
	v_exp_f32_e32 v12, v15
	v_cvt_pk_bf16_f32 v119, v7, v13
	v_cvt_pk_bf16_f32 v118, v6, v11
	v_cvt_pk_bf16_f32 v121, v9, v10
	v_cvt_pk_bf16_f32 v120, v8, v12
	s_waitcnt lgkmcnt(0)
	v_mfma_f32_32x32x16_f16 v[2:17], v[2:5], v[72:75], 0
	v_permlane16_swap_b32_e32 v106, v118
	v_permlane16_swap_b32_e32 v107, v119
	v_permlane16_swap_b32_e32 v108, v120
	v_permlane16_swap_b32_e32 v109, v121
	v_mfma_f32_32x32x16_f16 v[2:17], v[122:125], v[76:79], v[2:17]
	v_exp_f32_e32 v38, v20
	v_exp_f32_e32 v20, v22
	v_exp_f32_e32 v22, v24
	v_exp_f32_e32 v24, v25
	v_exp_f32_e32 v25, v21
	v_exp_f32_e32 v23, v23
	v_exp_f32_e32 v39, v19
	v_mfma_f32_16x16x32_bf16 v[84:87], v[114:117], v[106:109], v[84:87]
	v_cvt_pk_bf16_f32 v21, v22, v24
	v_cvt_pk_bf16_f32 v19, v38, v25
	v_exp_f32_e32 v22, v26
	v_mfma_f32_16x16x32_bf16 v[34:37], v[114:117], v[118:121], v[34:37]
	ds_read_b128 v[106:109], v89 offset:30720
	ds_read_b128 v[114:117], v89 offset:31744
	v_exp_f32_e32 v25, v32
	v_exp_f32_e32 v26, v33
	s_waitcnt lgkmcnt(1)
	v_mfma_f32_32x32x16_f16 v[2:17], v[106:109], v[80:83], v[2:17]
	v_exp_f32_e32 v18, v18
	v_cvt_pk_bf16_f32 v20, v20, v23
	v_exp_f32_e32 v23, v28
	v_exp_f32_e32 v24, v30
	v_exp_f32_e32 v28, v31
	v_exp_f32_e32 v29, v29
	v_exp_f32_e32 v27, v27
	v_cvt_pk_bf16_f32 v25, v25, v26
	s_nop 3
	v_exp_f32_e32 v26, v4
	v_exp_f32_e32 v4, v6
	v_exp_f32_e32 v6, v8
	v_exp_f32_e32 v8, v9
	v_exp_f32_e32 v7, v7
	v_exp_f32_e32 v9, v5
	v_cvt_pk_bf16_f32 v18, v18, v39
	v_cvt_pk_bf16_f32 v24, v24, v28
	v_cvt_pk_bf16_f32 v23, v23, v29
	v_cvt_pk_bf16_f32 v22, v22, v27
	v_exp_f32_e32 v2, v2
	v_exp_f32_e32 v27, v3
	v_cvt_pk_bf16_f32 v5, v6, v8
	v_cvt_pk_bf16_f32 v4, v4, v7
	v_cvt_pk_bf16_f32 v3, v26, v9
	v_exp_f32_e32 v6, v10
	v_exp_f32_e32 v7, v12
	v_exp_f32_e32 v8, v14
	v_exp_f32_e32 v9, v16
	v_exp_f32_e32 v10, v17
	v_exp_f32_e32 v12, v15
	v_exp_f32_e32 v13, v13
	v_exp_f32_e32 v11, v11
	v_permlane16_swap_b32_e32 v18, v22
	v_permlane16_swap_b32_e32 v19, v23
	v_permlane16_swap_b32_e32 v20, v24
	v_permlane16_swap_b32_e32 v21, v25
	v_cvt_pk_bf16_f32 v2, v2, v27
	s_nop 0
	v_mfma_f32_16x16x32_bf16 v[18:21], v[110:113], v[18:21], v[84:87]
	v_cvt_pk_bf16_f32 v9, v9, v10
	v_cvt_pk_bf16_f32 v8, v8, v12
	v_cvt_pk_bf16_f32 v7, v7, v13
	v_mfma_f32_16x16x32_bf16 v[22:25], v[110:113], v[22:25], v[34:37]
	v_cvt_pk_bf16_f32 v6, v6, v11
	s_nop 1
	v_permlane16_swap_b32_e32 v2, v6
	v_permlane16_swap_b32_e32 v3, v7
	v_permlane16_swap_b32_e32 v4, v8
	v_permlane16_swap_b32_e32 v5, v9
	s_waitcnt lgkmcnt(0)
	s_nop 0
	v_mfma_f32_16x16x32_bf16 v[84:87], v[114:117], v[2:5], v[18:21]
	s_waitcnt vmcnt(0)
	s_barrier
	v_mfma_f32_16x16x32_bf16 v[18:21], v[114:117], v[6:9], v[22:25]
	s_branch .LBB3_6
